# MoE-up full rounds: XCD owns all 8 column tiles of its 4 row tiles (unit i*256+perm(c)); last partial round keeps original mapping
# speedup vs baseline: 1.0125x; 1.0092x over previous
; __device__ __forceinline__ int otid() { int t = threadIdx.x; asm volatile("" : "+v"(t)); return t; }
;     __syncthreads();
;     const int tid = otid();
;     if (tid == 0) { int t = 0; for (int e = 0; e < 32; ++e) { tab[TAB_TPRE + e] = t; tab[TAB_OFFP + e] = t * 256; tab[TAB_CNT + e] = cnt[e]; t += (cnt[e] + 255) >> 8; } tab[TAB_TPRE + 32] = t; tab[TAB_OFFP + 32] = t * 256; }
;     __syncthreads();
;     if (ntn > 0 && tid < 32) {
;         const int total = tab[TAB_TPRE + 32] * ntn; int v = -1;
;         int Lx = tid * G + c;
;         if (ntn == 4 && G == 256) { const int x = c & 7, j = c >> 3; Lx = (tid * 64 + x * 8 + (j >> 2)) * 4 + (j & 3); }
;         if (Lx < total) { const int tile = Lx / ntn, pn = Lx % ntn; int e = 0; for (int k = 1; k < 32; ++k) e += (tab[TAB_TPRE + k] <= tile) ? 1 : 0; v = (e << 24) | ((tile - tab[TAB_TPRE + e]) << 8) | pn; }
;         tab[TAB_UNIT + tid] = v; tab[TAB_LX + tid] = Lx;
.LBB0_1661:
	s_or_b64 exec, exec, s[0:1]
	v_cmp_gt_i32_e32 vcc, 32, v1
	s_waitcnt lgkmcnt(0)
	s_barrier
	s_and_saveexec_b64 s[0:1], vcc
	s_cbranch_execz .LBB0_1665
	v_readlane_b32 s4, v254, 16
	s_nop 1
	v_mov_b32_e32 v2, s4
	ds_read_b32 v4, v2
	v_mul_lo_u32 v2, v1, s88
	s_and_b32 s72, s86, 7
	s_lshl_b32 s72, s72, 5
	s_bfe_u32 s73, s86, 0x20006
	s_lshl_b32 s73, s73, 3
	s_or_b32 s72, s72, s73
	s_bfe_u32 s73, s86, 0x30003
	s_or_b32 s72, s72, s73
	s_cmp_eq_u32 s88, 0x100
	s_cselect_b32 s72, s72, s86
	s_waitcnt lgkmcnt(0)
	v_lshlrev_b32_e32 v4, 3, v4
	v_add_u32_e32 v5, 0x100, v2
	v_cmp_gt_i32_e32 vcc, v5, v4
	v_mov_b32_e32 v6, s86
	v_mov_b32_e32 v7, s72
	s_nop 0
	v_cndmask_b32_e32 v6, v7, v6, vcc
	v_add_u32_e32 v2, v2, v6
	v_cmp_lt_i32_e32 vcc, v2, v4
	v_mov_b32_e32 v4, -1
	s_and_saveexec_b64 s[6:7], vcc
	s_cbranch_execz .LBB0_1664
	v_readlane_b32 s4, v254, 37
	v_ashrrev_i32_e32 v4, 31, v2
	v_lshrrev_b32_e32 v4, 29, v4
	v_mov_b32_e32 v6, s4
	ds_read2_b32 v[6:7], v6 offset1:1
	v_add_u32_e32 v5, v2, v4
	v_ashrrev_i32_e32 v4, 3, v5
	v_readlane_b32 s4, v254, 38
	v_and_b32_e32 v5, -8, v5
	s_waitcnt lgkmcnt(0)
	v_cmp_le_i32_e32 vcc, v6, v4
	v_mov_b32_e32 v6, s4
	v_readlane_b32 s4, v254, 39
	v_cndmask_b32_e64 v8, 0, 1, vcc
	v_cmp_le_i32_e32 vcc, v7, v4
	ds_read2_b32 v[6:7], v6 offset1:1
	v_sub_u32_e32 v5, v2, v5
	v_cndmask_b32_e64 v9, 0, 1, vcc
	s_waitcnt lgkmcnt(0)
	v_cmp_le_i32_e32 vcc, v6, v4
	s_nop 1
	v_addc_co_u32_e32 v8, vcc, v9, v8, vcc
	v_mov_b32_e32 v6, s4
	v_cmp_le_i32_e32 vcc, v7, v4
	ds_read2_b32 v[6:7], v6 offset1:1
	v_readlane_b32 s4, v254, 40
	v_cndmask_b32_e64 v9, 0, 1, vcc
	s_waitcnt lgkmcnt(0)
	v_cmp_le_i32_e32 vcc, v6, v4
	s_nop 1
	v_addc_co_u32_e32 v8, vcc, v8, v9, vcc
	v_mov_b32_e32 v6, s4
	v_cmp_le_i32_e32 vcc, v7, v4
	ds_read2_b32 v[6:7], v6 offset1:1
	v_readlane_b32 s4, v254, 41
	v_cndmask_b32_e64 v9, 0, 1, vcc
	s_waitcnt lgkmcnt(0)
	v_cmp_le_i32_e32 vcc, v6, v4
	s_nop 1
	v_addc_co_u32_e32 v8, vcc, v8, v9, vcc
	v_mov_b32_e32 v6, s4
	v_cmp_le_i32_e32 vcc, v7, v4
	ds_read2_b32 v[6:7], v6 offset1:1
	v_readlane_b32 s4, v254, 42
	v_cndmask_b32_e64 v9, 0, 1, vcc
	s_waitcnt lgkmcnt(0)
	v_cmp_le_i32_e32 vcc, v6, v4
	s_nop 1
	v_addc_co_u32_e32 v8, vcc, v8, v9, vcc
	v_mov_b32_e32 v6, s4
	v_cmp_le_i32_e32 vcc, v7, v4
	ds_read2_b32 v[6:7], v6 offset1:1
	v_readlane_b32 s4, v254, 43
	v_cndmask_b32_e64 v9, 0, 1, vcc
	s_waitcnt lgkmcnt(0)
	v_cmp_le_i32_e32 vcc, v6, v4
	s_nop 1
	v_addc_co_u32_e32 v8, vcc, v8, v9, vcc
	v_mov_b32_e32 v6, s4
	v_cmp_le_i32_e32 vcc, v7, v4
	ds_read2_b32 v[6:7], v6 offset1:1
	v_readlane_b32 s4, v254, 44
	v_cndmask_b32_e64 v9, 0, 1, vcc
	s_waitcnt lgkmcnt(0)
	v_cmp_le_i32_e32 vcc, v6, v4
	s_nop 1
	v_addc_co_u32_e32 v8, vcc, v8, v9, vcc
	v_mov_b32_e32 v6, s4
	v_cmp_le_i32_e32 vcc, v7, v4
	ds_read2_b32 v[6:7], v6 offset1:1
	v_readlane_b32 s4, v254, 45
	v_cndmask_b32_e64 v9, 0, 1, vcc
	s_waitcnt lgkmcnt(0)
	v_cmp_le_i32_e32 vcc, v6, v4
	s_nop 1
	v_addc_co_u32_e32 v8, vcc, v8, v9, vcc
	v_mov_b32_e32 v6, s4
	v_cmp_le_i32_e32 vcc, v7, v4
	ds_read2_b32 v[6:7], v6 offset1:1
	v_readlane_b32 s4, v254, 46
	v_cndmask_b32_e64 v9, 0, 1, vcc
	s_waitcnt lgkmcnt(0)
	v_cmp_le_i32_e32 vcc, v6, v4
	s_nop 1
	v_addc_co_u32_e32 v8, vcc, v8, v9, vcc
	v_mov_b32_e32 v6, s4
	v_cmp_le_i32_e32 vcc, v7, v4
	ds_read2_b32 v[6:7], v6 offset1:1
	v_readlane_b32 s4, v254, 47
	v_cndmask_b32_e64 v9, 0, 1, vcc
	s_waitcnt lgkmcnt(0)
	v_cmp_le_i32_e32 vcc, v6, v4
	s_nop 1
	v_addc_co_u32_e32 v8, vcc, v8, v9, vcc
	v_mov_b32_e32 v6, s4
	v_cmp_le_i32_e32 vcc, v7, v4
	ds_read2_b32 v[6:7], v6 offset1:1
	v_readlane_b32 s4, v254, 48
	v_cndmask_b32_e64 v9, 0, 1, vcc
	s_waitcnt lgkmcnt(0)
	v_cmp_le_i32_e32 vcc, v6, v4
	s_nop 1
	v_addc_co_u32_e32 v8, vcc, v8, v9, vcc
	v_mov_b32_e32 v6, s4
	v_cmp_le_i32_e32 vcc, v7, v4
	ds_read2_b32 v[6:7], v6 offset1:1
	v_readlane_b32 s4, v254, 49
	v_cndmask_b32_e64 v9, 0, 1, vcc
	s_waitcnt lgkmcnt(0)
	v_cmp_le_i32_e32 vcc, v6, v4
	s_nop 1
	v_addc_co_u32_e32 v8, vcc, v8, v9, vcc
	v_mov_b32_e32 v6, s4
	v_cmp_le_i32_e32 vcc, v7, v4
	ds_read2_b32 v[6:7], v6 offset1:1
	v_readlane_b32 s4, v254, 50
	v_cndmask_b32_e64 v9, 0, 1, vcc
	s_waitcnt lgkmcnt(0)
	v_cmp_le_i32_e32 vcc, v6, v4
	s_nop 1
	v_addc_co_u32_e32 v8, vcc, v8, v9, vcc
	v_mov_b32_e32 v6, s4
	v_cmp_le_i32_e32 vcc, v7, v4
	ds_read2_b32 v[6:7], v6 offset1:1
	v_readlane_b32 s4, v254, 51
	v_cndmask_b32_e64 v9, 0, 1, vcc
	s_waitcnt lgkmcnt(0)
	v_cmp_le_i32_e32 vcc, v6, v4
	s_nop 1
	v_addc_co_u32_e32 v8, vcc, v8, v9, vcc
	v_mov_b32_e32 v6, s4
	v_cmp_le_i32_e32 vcc, v7, v4
	ds_read2_b32 v[6:7], v6 offset1:1
	v_readlane_b32 s4, v254, 52
	v_cndmask_b32_e64 v9, 0, 1, vcc
	s_waitcnt lgkmcnt(0)
	v_cmp_le_i32_e32 vcc, v6, v4
	s_nop 1
	v_addc_co_u32_e32 v6, vcc, v8, v9, vcc
	v_mov_b32_e32 v8, s4
	ds_read_b32 v8, v8
	v_cmp_le_i32_e32 vcc, v7, v4
	s_nop 1
	v_cndmask_b32_e64 v7, 0, 1, vcc
	s_waitcnt lgkmcnt(0)
	v_cmp_le_i32_e32 vcc, v8, v4
	s_nop 1
	v_addc_co_u32_e32 v6, vcc, v6, v7, vcc
	v_lshlrev_b32_e32 v7, 24, v6
	v_lshl_add_u32 v6, v6, 2, 0
	v_add_u32_e32 v6, 0x20000, v6
	ds_read_b32 v6, v6
	s_waitcnt lgkmcnt(0)
	v_sub_u32_e32 v4, v4, v6
	v_lshlrev_b32_e32 v4, 8, v4
	v_or3_b32 v4, v4, v5, v7
